# P7 B operand staged via registers + ds_write instead of LDS-DMA (halves DMA bytes in P7 K-loop)
# baseline (speedup 1.0000x reference)
; __device__ __forceinline__ int ltid(int wave0) { int t; asm volatile("v_mbcnt_lo_u32_b32 %0, -1, 0\n\tv_mbcnt_hi_u32_b32 %0, -1, %0" : "=v"(t)); return (wave0 << 6) | t; }
; #define PG8_STAGE_B(bufoff, gbase) do { _Pragma("unroll") for (int _i = 0; _i < 2; ++_i) \
;         __builtin_amdgcn_global_load_lds((const unsigned*)((const char*)(gbase) + voffB[_i]), (LAS unsigned*)(lds + (bufoff) + ldsw + _i * 8192), 16, 0, 0); } while (0)
; #define PG8_STAGE_A(bufoff, gbase, VO, h) do { _Pragma("unroll") for (int _i = 0; _i < 2; ++_i) \
;         __builtin_amdgcn_global_load_lds((const unsigned*)((const char*)(gbase) + (VO)[h][_i]), (LAS unsigned*)(lds + (bufoff) + ldsw + _i * 8192), 16, 0, 0); } while (0)
; #define PG8_BAR __builtin_amdgcn_s_barrier()
;     ...
;     const int tid = ltid(wave0), wid = wave0, lane = tid & 63, wr = wid >> 2, wc = wid & 3, fr = lane & 15, fq = lane >> 4;
;     const int nt = K / BK;
;     unsigned voffB[2], voffA[2][2], voffN[2][2]; int Rr[2], Cc[2];
; #pragma unroll
;     for (int i = 0; i < 2; ++i) { int R, C; stage_rc(tid * 16 + i * 8192, R, C); const int Rb = (R & ~31) + perm32(R & 31);
;         Rr[i] = R; Cc[i] = C; voffB[i] = nB64 ? (unsigned)(Rb * 64 + ((C * 2) & 63) + ((C * 2) >> 6) * nB64 * 64) : (unsigned)(Rb * ldb + C) * 2u;
;         voffA[0][i] = (unsigned)(R * lda + C) * 2u; voffA[1][i] = (unsigned)((R + HALF) * lda + C) * 2u; voffN[0][i] = voffA[0][i]; voffN[1][i] = voffA[1][i]; }
;     ...
;     const char* cA = cur.A; const char* cB = cur.B;
;     PG8_STAGE_B(PG8_SB(0, 0), cB); PG8_STAGE_B(PG8_SB(0, 1), cB + hstepB); PG8_STAGE_A(PG8_SA(0, 0), cA, voffA, 0); PG8_STAGE_A(PG8_SA(0, 1), cA, voffA, 1);
;     if (wr == 1) PG8_BAR;
.LBB0_1401:
	v_readlane_b32 s0, v254, 12
	v_mbcnt_lo_u32_b32 v0, -1, 0
	v_mbcnt_hi_u32_b32 v0, -1, v0
	s_nop 1
	v_mov_b32_e32 v1, s0
	ds_read_b32 v1, v1
	v_readlane_b32 s0, v249, 2
	s_waitcnt lgkmcnt(0)
	v_lshlrev_b32_e32 v1, 3, v1
	v_cmp_ge_i32_e32 vcc, s0, v1
	s_cbranch_vccnz .LBB0_1431
	v_readlane_b32 s4, v249, 40
	v_mov_b32_e32 v7, 0x10000
	s_mov_b32 s3, 0xfffe0000
	v_lshl_or_b32 v1, v0, 4, s4
	v_add_u32_e32 v248, 0x10000, v1
	v_add_u32_e32 v2, 0x2000, v1
	v_ashrrev_i32_e32 v3, 31, v2
	v_lshrrev_b32_e32 v3, 22, v3
	v_add_u32_e32 v3, v2, v3
	v_ashrrev_i32_e32 v3, 10, v3
	v_mul_i32_i24_e32 v4, 0x400, v3
	v_sub_u32_e32 v2, v2, v4
	v_lshrrev_b32_e32 v4, 4, v2
	v_bitop3_b32 v2, v4, v2, 32 bitop3:0x6c
	v_ashrrev_i32_e32 v4, 31, v2
	v_lshrrev_b32_e32 v4, 26, v4
	v_add_u32_e32 v4, v2, v4
	v_ashrrev_i32_e32 v5, 6, v4
	v_and_b32_e32 v4, 0xffc0, v4
	v_sub_u32_e32 v2, v2, v4
	v_lshrrev_b16_e32 v4, 7, v2
	v_and_b32_e32 v4, 1, v4
	v_lshlrev_b32_e32 v6, 3, v3
	v_lshlrev_b32_e32 v3, 5, v3
	v_add_u16_e32 v2, v2, v4
	v_and_b32_e32 v6, -16, v6
	v_and_b32_e32 v3, 32, v3
	v_ashrrev_i16_sdwa v2, v222, sext(v2) dst_sel:DWORD dst_unused:UNUSED_PAD src0_sel:DWORD src1_sel:BYTE_0
	v_add_u32_e32 v6, v5, v6
	v_add_u32_sdwa v2, v3, sext(v2) dst_sel:DWORD dst_unused:UNUSED_PAD src0_sel:DWORD src1_sel:WORD_0
	v_lshl_add_u32 v3, v6, 8, v2
	v_lshl_add_u32 v194, v3, 1, v7
	v_lshlrev_b32_e32 v3, 1, v2
	v_lshl_add_u32 v196, v6, 9, v3
	v_lshlrev_b32_e32 v2, 12, v2
	v_and_b32_e32 v3, 62, v3
	v_and_or_b32 v2, v2, s3, v3
	v_and_b32_e32 v3, 3, v5
	s_mov_b32 s2, 0x3ffffe0
	v_lshrrev_b32_e32 v4, 2, v6
	v_lshlrev_b32_e32 v5, 1, v6
	v_and_or_b32 v3, v6, s2, v3
	v_and_b32_e32 v4, 4, v4
	v_and_b32_e32 v5, 24, v5
	v_or3_b32 v3, v3, v4, v5
	v_lshl_add_u32 v198, v3, 6, v2
	v_and_b32_e32 v9, -32, v6
	v_lshl_add_u32 v198, v9, 6, v198
	v_and_b32_e32 v9, 12, v6
	v_lshl_add_u32 v198, v9, 7, v198
	v_ashrrev_i32_e32 v2, 31, v1
	v_lshrrev_b32_e32 v2, 22, v2
	v_add_u32_e32 v2, v1, v2
	v_ashrrev_i32_e32 v2, 10, v2
	v_mul_i32_i24_e32 v3, 0x400, v2
	v_sub_u32_e32 v1, v1, v3
	v_lshrrev_b32_e32 v3, 4, v1
	v_bitop3_b32 v1, v3, v1, 32 bitop3:0x6c
	v_ashrrev_i32_e32 v3, 31, v1
	v_lshrrev_b32_e32 v3, 26, v3
	v_add_u32_e32 v3, v1, v3
	v_ashrrev_i32_e32 v4, 6, v3
	v_and_b32_e32 v3, 0xc0, v3
	v_lshlrev_b32_e32 v5, 3, v2
	v_lshlrev_b32_e32 v2, 5, v2
	v_sub_u32_e32 v1, v1, v3
	v_and_b32_e32 v5, -16, v5
	v_and_b32_e32 v2, 32, v2
	v_ashrrev_i16_sdwa v1, v222, sext(v1) dst_sel:DWORD dst_unused:UNUSED_PAD src0_sel:DWORD src1_sel:BYTE_0
	v_add_u32_e32 v5, v4, v5
	v_add_u32_sdwa v1, v2, sext(v1) dst_sel:DWORD dst_unused:UNUSED_PAD src0_sel:DWORD src1_sel:WORD_0
	v_readlane_b32 s0, v254, 22
	v_lshl_add_u32 v2, v5, 8, v1
	s_add_u32 s31, s0, 0x14800000
	v_readlane_b32 s0, v254, 23
	v_lshl_add_u32 v200, v2, 1, v7
	v_lshlrev_b32_e32 v2, 1, v1
	s_addc_u32 s34, s0, 0
	v_readlane_b32 s0, v251, 43
	v_lshl_add_u32 v202, v5, 9, v2
	v_lshlrev_b32_e32 v1, 12, v1
	v_and_b32_e32 v2, 62, v2
	v_readlane_b32 s1, v251, 44
	s_add_u32 s0, s31, s0
	v_and_or_b32 v1, v1, s3, v2
	v_and_b32_e32 v2, 3, v4
	v_lshrrev_b32_e32 v3, 2, v5
	v_lshlrev_b32_e32 v4, 1, v5
	v_readlane_b32 s3, v251, 40
	s_addc_u32 s1, s34, s1
	v_and_or_b32 v2, v5, s2, v2
	v_and_b32_e32 v3, 4, v3
	v_and_b32_e32 v4, 24, v4
	s_add_i32 s2, s3, 0
	v_or3_b32 v2, v2, v3, v4
	s_add_i32 s2, s2, 0x23320
	v_lshl_add_u32 v64, v2, 6, v1
	v_and_b32_e32 v9, -32, v5
	v_lshl_add_u32 v64, v9, 6, v64
	v_and_b32_e32 v9, 12, v5
	v_lshl_add_u32 v64, v9, 7, v64
	v_mov_b32_e32 v1, s2
	ds_read_u8 v1, v1
	s_waitcnt lgkmcnt(0)
	v_lshlrev_b32_e32 v2, 2, v1
	v_add_u32_e32 v2, 0, v2
	v_add_u32_e32 v3, 0x2320c, v2
	ds_read_b32 v3, v3
	v_add_u32_e32 v2, 0x23104, v2
	ds_read_b32 v2, v2
	s_waitcnt lgkmcnt(0)
	v_readfirstlane_b32 s2, v3
	s_sub_i32 s2, s3, s2
	s_lshl_b32 s2, s2, 8
	v_readfirstlane_b32 s3, v2
	s_add_i32 s12, s2, s3
	v_readfirstlane_b32 s2, v1
	s_lshl_b32 s2, s2, 20
	s_add_u32 s14, s0, s2
	s_addc_u32 s15, s1, 0
	s_ashr_i32 s13, s12, 31
	s_lshl_b64 s[0:1], s[12:13], 9
	v_readlane_b32 s2, v251, 32
	v_readlane_b32 s3, v251, 33
	s_add_u32 s16, s2, s0
	s_addc_u32 s17, s3, s1
	s_add_i32 s13, s4, 0
	s_add_i32 s35, s13, 0x10000
	s_add_i32 s36, s13, 0x12000
	s_mov_b32 m0, s35
	s_add_u32 s0, s14, 0x200
	global_load_lds_dwordx4 v64, s[14:15]
	s_mov_b32 m0, s36
	s_addc_u32 s1, s15, 0
	s_add_i32 s37, s13, 0x14000
	global_load_lds_dwordx4 v198, s[14:15]
	s_mov_b32 m0, s37
	s_add_i32 s38, s13, 0x16000
	global_load_lds_dwordx4 v64, s[0:1]
	s_mov_b32 m0, s38
	s_add_i32 s39, s13, 0x2000
	global_load_lds_dwordx4 v198, s[0:1]
	s_mov_b32 m0, s13
	s_add_i32 s40, s13, 0x4000
	global_load_lds_dwordx4 v202, s[16:17]
	s_mov_b32 m0, s39
	s_add_i32 s41, s13, 0x6000
	global_load_lds_dwordx4 v196, s[16:17]
	s_mov_b32 m0, s40
	v_readlane_b32 s2, v249, 47
	global_load_lds_dwordx4 v200, s[16:17]
	s_mov_b32 m0, s41
	v_readlane_b32 s3, v249, 48
	global_load_lds_dwordx4 v194, s[16:17]
	s_nop 0
	v_cndmask_b32_e64 v1, 0, 1, s[2:3]
	v_cmp_ne_u32_e64 s[0:1], 1, v1
	s_andn2_b64 vcc, exec, s[2:3]
	s_cbranch_vccnz .LBB0_1404
	s_barrier
; #define PG8_STAGE_B(bufoff, gbase) do { _Pragma("unroll") for (int _i = 0; _i < 2; ++_i) \
;         __builtin_amdgcn_global_load_lds((const unsigned*)((const char*)(gbase) + voffB[_i]), (LAS unsigned*)(lds + (bufoff) + ldsw + _i * 8192), 16, 0, 0); } while (0)
; #define PG8_STAGE_A(bufoff, gbase, VO, h) do { _Pragma("unroll") for (int _i = 0; _i < 2; ++_i) \
;         __builtin_amdgcn_global_load_lds((const unsigned*)((const char*)(gbase) + (VO)[h][_i]), (LAS unsigned*)(lds + (bufoff) + ldsw + _i * 8192), 16, 0, 0); } while (0)
; #define PG8_WAIT_V(n) asm volatile("s_waitcnt vmcnt(" #n ")" ::: "memory")
; #define PG8_BAR __builtin_amdgcn_s_barrier()
;     ...
;     PG8_STAGE_B(PG8_SB(1, 0), cB + kstepB); PG8_STAGE_A(PG8_SA(1, 0), cA + kstep, voffA, 0); PG8_STAGE_B(PG8_SB(1, 1), cB + hstepB + kstepB);
;     PG8_WAIT_V(6); PG8_BAR;
.LBB0_1404:
	v_and_b32_e32 v1, 15, v0
	v_readlane_b32 s2, v249, 41
	v_lshrrev_b32_e32 v6, 1, v0
	v_and_b32_e32 v6, 24, v6
	v_or_b32_e32 v210, s2, v1
	v_lshlrev_b32_e32 v7, 6, v210
	v_lshlrev_b32_e32 v8, 1, v6
	s_movk_i32 s2, 0x3c0
	v_lshlrev_b32_e32 v9, 2, v210
	v_and_or_b32 v7, v7, s2, v8
	v_and_b32_e32 v9, 32, v9
	v_readlane_b32 s2, v249, 42
	v_lshlrev_b32_e32 v0, 2, v0
	v_lshl_or_b32 v1, v1, 6, v8
	v_bitop3_b32 v7, v7, s2, v9 bitop3:0xde
	v_and_b32_e32 v0, 32, v0
	v_readlane_b32 s2, v249, 44
	v_mov_b32_e32 v199, v65
	v_mov_b32_e32 v203, v65
	v_bitop3_b32 v8, v1, s2, v0 bitop3:0xde
	s_add_u32 s2, s14, 0x40000
	s_addc_u32 s3, s15, 0
	s_add_i32 s42, s13, 0x18000
	v_lshl_add_u64 v[0:1], s[2:3], 0, v[64:65]
	s_mov_b32 m0, s42
	s_add_i32 s43, s13, 0x1a000
	v_lshl_add_u64 v[2:3], s[16:17], 0, v[202:203]
	v_mov_b32_e32 v197, v65
	s_waitcnt vmcnt(2)
	s_barrier
	global_load_dwordx4 v[232:235], v[0:1], off
	v_lshl_add_u64 v[0:1], s[2:3], 0, v[198:199]
	s_add_i32 s44, s13, 0x8000
	s_add_i32 s45, s13, 0xa000
	v_lshl_add_u64 v[4:5], s[16:17], 0, v[196:197]
	global_load_dwordx4 v[236:239], v[0:1], off
	s_add_u32 s2, s14, 0x40200
	s_addc_u32 s3, s15, 0
	s_add_i32 s46, s13, 0x1c000
	s_add_i32 s47, s13, 0x1e000
	v_lshl_add_u64 v[0:1], s[2:3], 0, v[64:65]
	s_nop 0
	global_load_dwordx4 v[240:243], v[0:1], off
	v_lshl_add_u64 v[0:1], s[2:3], 0, v[198:199]
	s_nop 0
	global_load_dwordx4 v[244:247], v[0:1], off
	v_lshl_add_u64 v[0:1], v[2:3], 0, s[94:95]
	s_mov_b32 m0, s44
	s_nop 0
	global_load_lds_dwordx4 v[0:1], off
	v_lshl_add_u64 v[0:1], v[4:5], 0, s[94:95]
	s_mov_b32 m0, s45
	v_readlane_b32 s2, v249, 43
	global_load_lds_dwordx4 v[0:1], off
	s_waitcnt vmcnt(6)
	s_nop 0
	v_or_b32_e32 v204, s2, v6
	v_readlane_b32 s2, v251, 41
	v_mov_b32_e32 v201, v65
	v_mov_b32_e32 v195, v65
	v_mov_b32_e32 v205, v65
	s_mov_b32 s48, 0
	s_mov_b64 s[18:19], 0
	v_add_u32_e32 v211, 0, v8
	v_add_u32_e32 v212, 0, v7
	s_mov_b32 s49, s2
	s_mov_b64 s[8:9], s[14:15]
	s_mov_b64 s[10:11], s[16:17]
	s_barrier
	v_readlane_b32 s3, v251, 42
	s_branch .LBB0_1407

; #define PG8_STAGE_B(bufoff, gbase) do { _Pragma("unroll") for (int _i = 0; _i < 2; ++_i) \
;         __builtin_amdgcn_global_load_lds((const unsigned*)((const char*)(gbase) + voffB[_i]), (LAS unsigned*)(lds + (bufoff) + ldsw + _i * 8192), 16, 0, 0); } while (0)
; #define PG8_STAGE_A(bufoff, gbase, VO, h) do { _Pragma("unroll") for (int _i = 0; _i < 2; ++_i) \
;         __builtin_amdgcn_global_load_lds((const unsigned*)((const char*)(gbase) + (VO)[h][_i]), (LAS unsigned*)(lds + (bufoff) + ldsw + _i * 8192), 16, 0, 0); } while (0)
; #define PG8_WAIT_V(n) asm volatile("s_waitcnt vmcnt(" #n ")" ::: "memory")
; #define PG8_WAIT_L(n) asm volatile("s_waitcnt lgkmcnt(" #n ")" ::: "memory")
; #define PG8_WAIT_VX(rx) do { if (rx) asm volatile("s_waitcnt vmcnt(%0)" :: "n"(8 + Epi::NVM) : "memory"); else asm volatile("s_waitcnt vmcnt(8)" ::: "memory"); } while (0)
; #define PG8_BAR __builtin_amdgcn_s_barrier()
; #define PG8_SCHED __builtin_amdgcn_sched_barrier(0)
;     ...
;             PG8_WAIT_VX(rx); PG8_WAIT_L(0); PG8_BAR; PG8_MMA(0, 0, At, B0); PG8_MMA(0, 1, At, B1); PG8_BAR; PG8_SCHED;
;             PG8_LDA(At, 1, 1); PG8_STAGE_B(PG8_SB(1, 0), b3); PG8_STAGE_B(PG8_SB(1, 1), b3 + hstepB); PG8_STAGE_A(PG8_SA(1, 0), a3, vo2, 0);
;             PG8_WAIT_V(8); PG8_WAIT_L(0); PG8_BAR; PG8_MMA(1, 0, At, B0); PG8_MMA(1, 1, At, B1); PG8_BAR; PG8_SCHED;
.LBB0_1410:
	s_xor_b64 s[26:27], s[22:23], -1
	s_waitcnt lgkmcnt(0)
	s_add_u32 s2, s24, 0x40000
	s_addc_u32 s3, s25, 0
	s_barrier
	s_setprio 1
	s_waitcnt lgkmcnt(0)
	v_mfma_scale_f32_16x16x128_f8f6f4 v[190:193], v[24:31], v[56:63], v[190:193], v226, v228 op_sel_hi:[0,0,0]
	v_mfma_scale_f32_16x16x128_f8f6f4 v[186:189], v[16:23], v[56:63], v[186:189], v226, v228 op_sel_hi:[0,0,0]
	v_mfma_scale_f32_16x16x128_f8f6f4 v[178:181], v[24:31], v[48:55], v[178:181], v226, v228 op_sel_hi:[0,0,0]
	v_mfma_scale_f32_16x16x128_f8f6f4 v[170:173], v[16:23], v[48:55], v[170:173], v226, v228 op_sel_hi:[0,0,0]
	v_mfma_scale_f32_16x16x128_f8f6f4 v[162:165], v[24:31], v[40:47], v[162:165], v226, v228 op_sel_hi:[0,0,0]
	v_mfma_scale_f32_16x16x128_f8f6f4 v[154:157], v[16:23], v[40:47], v[154:157], v226, v228 op_sel_hi:[0,0,0]
	v_mfma_scale_f32_16x16x128_f8f6f4 v[146:149], v[24:31], v[32:39], v[146:149], v226, v228 op_sel_hi:[0,0,0]
	v_mfma_scale_f32_16x16x128_f8f6f4 v[138:141], v[16:23], v[32:39], v[138:141], v226, v228 op_sel_hi:[0,0,0]
	s_setprio 0
	s_setprio 1
	v_mfma_scale_f32_16x16x128_f8f6f4 v[182:185], v[8:15], v[56:63], v[182:185], v226, v228 op_sel_hi:[0,0,0]
	v_mfma_scale_f32_16x16x128_f8f6f4 v[174:177], v[0:7], v[56:63], v[174:177], v226, v228 op_sel_hi:[0,0,0]
	v_mfma_scale_f32_16x16x128_f8f6f4 v[166:169], v[8:15], v[48:55], v[166:169], v226, v228 op_sel_hi:[0,0,0]
	v_mfma_scale_f32_16x16x128_f8f6f4 v[158:161], v[0:7], v[48:55], v[158:161], v226, v228 op_sel_hi:[0,0,0]
	v_mfma_scale_f32_16x16x128_f8f6f4 v[150:153], v[8:15], v[40:47], v[150:153], v226, v228 op_sel_hi:[0,0,0]
	v_mfma_scale_f32_16x16x128_f8f6f4 v[142:145], v[0:7], v[40:47], v[142:145], v226, v228 op_sel_hi:[0,0,0]
	v_mfma_scale_f32_16x16x128_f8f6f4 v[134:137], v[8:15], v[32:39], v[134:137], v226, v228 op_sel_hi:[0,0,0]
	v_mfma_scale_f32_16x16x128_f8f6f4 v[130:133], v[0:7], v[32:39], v[130:133], v226, v228 op_sel_hi:[0,0,0]
	s_setprio 0
	s_barrier
	s_mov_b32 m0, s42
	v_lshl_add_u64 v[214:215], s[2:3], 0, v[64:65]
	ds_read_b128 v[32:35], v212 offset:49152
	ds_read_b128 v[36:39], v212 offset:50176
	ds_read_b128 v[40:43], v212 offset:51200
	ds_read_b128 v[44:47], v212 offset:52224
	ds_read_b128 v[48:51], v212 offset:53248
	ds_read_b128 v[52:55], v212 offset:54272
	ds_read_b128 v[56:59], v212 offset:55296
	ds_read_b128 v[60:63], v212 offset:56320
	s_waitcnt vmcnt(4)
	ds_write_b128 v248, v[232:235]
	ds_write_b128 v248, v[236:239] offset:8192
	ds_write_b128 v248, v[240:243] offset:16384
	ds_write_b128 v248, v[244:247] offset:24576
	global_load_dwordx4 v[232:235], v[214:215], off
	v_lshl_add_u64 v[214:215], s[2:3], 0, v[198:199]
	s_add_u32 s2, s24, 0x40200
	s_mov_b32 m0, s43
	s_addc_u32 s3, s25, 0
	global_load_dwordx4 v[236:239], v[214:215], off
	v_lshl_add_u64 v[214:215], s[2:3], 0, v[64:65]
	s_mov_b32 m0, s46
	v_lshl_add_u64 v[206:207], v[206:207], 0, s[94:95]
	global_load_dwordx4 v[240:243], v[214:215], off
	v_lshl_add_u64 v[214:215], s[2:3], 0, v[198:199]
	s_mov_b32 m0, s47
	s_nop 0
	global_load_dwordx4 v[244:247], v[214:215], off
	s_mov_b32 m0, s44
	s_nop 0
	global_load_lds_dwordx4 v[206:207], off
	v_lshl_add_u64 v[206:207], v[208:209], 0, s[94:95]
	s_mov_b32 m0, s45
	s_nop 0
	global_load_lds_dwordx4 v[206:207], off
	s_waitcnt vmcnt(8)
	s_waitcnt lgkmcnt(0)
	s_barrier
	s_setprio 1
	s_waitcnt lgkmcnt(0)
	v_mfma_scale_f32_16x16x128_f8f6f4 v[126:129], v[24:31], v[32:39], v[126:129], v226, v228 op_sel_hi:[0,0,0]
	v_mfma_scale_f32_16x16x128_f8f6f4 v[122:125], v[16:23], v[32:39], v[122:125], v226, v228 op_sel_hi:[0,0,0]
	v_mfma_scale_f32_16x16x128_f8f6f4 v[114:117], v[24:31], v[40:47], v[114:117], v226, v228 op_sel_hi:[0,0,0]
	v_mfma_scale_f32_16x16x128_f8f6f4 v[106:109], v[16:23], v[40:47], v[106:109], v226, v228 op_sel_hi:[0,0,0]
	v_mfma_scale_f32_16x16x128_f8f6f4 v[90:93], v[24:31], v[48:55], v[90:93], v226, v228 op_sel_hi:[0,0,0]
	v_mfma_scale_f32_16x16x128_f8f6f4 v[82:85], v[16:23], v[48:55], v[82:85], v226, v228 op_sel_hi:[0,0,0]
	v_mfma_scale_f32_16x16x128_f8f6f4 v[70:73], v[24:31], v[56:63], v[70:73], v226, v228 op_sel_hi:[0,0,0]
	v_mfma_scale_f32_16x16x128_f8f6f4 v[66:69], v[16:23], v[56:63], v[66:69], v226, v228 op_sel_hi:[0,0,0]
	s_setprio 0
	s_setprio 1
	v_mfma_scale_f32_16x16x128_f8f6f4 v[118:121], v[8:15], v[32:39], v[118:121], v226, v228 op_sel_hi:[0,0,0]
	v_mfma_scale_f32_16x16x128_f8f6f4 v[110:113], v[0:7], v[32:39], v[110:113], v226, v228 op_sel_hi:[0,0,0]
	v_mfma_scale_f32_16x16x128_f8f6f4 v[94:97], v[8:15], v[40:47], v[94:97], v226, v228 op_sel_hi:[0,0,0]
	v_mfma_scale_f32_16x16x128_f8f6f4 v[86:89], v[0:7], v[40:47], v[86:89], v226, v228 op_sel_hi:[0,0,0]
	v_mfma_scale_f32_16x16x128_f8f6f4 v[102:105], v[8:15], v[48:55], v[102:105], v226, v228 op_sel_hi:[0,0,0]
	v_mfma_scale_f32_16x16x128_f8f6f4 v[98:101], v[0:7], v[48:55], v[98:101], v226, v228 op_sel_hi:[0,0,0]
	v_mfma_scale_f32_16x16x128_f8f6f4 v[78:81], v[8:15], v[56:63], v[78:81], v226, v228 op_sel_hi:[0,0,0]
	v_mfma_scale_f32_16x16x128_f8f6f4 v[74:77], v[0:7], v[56:63], v[74:77], v226, v228 op_sel_hi:[0,0,0]
	s_setprio 0
	s_barrier
	s_mov_b32 s5, 2
	s_mov_b64 s[22:23], 0
	s_mov_b64 s[2:3], -1
	s_and_b64 vcc, exec, s[26:27]
	s_cbranch_vccnz .LBB0_1423

; #define PG8_STAGE_B(bufoff, gbase) do { _Pragma("unroll") for (int _i = 0; _i < 2; ++_i) \
;         __builtin_amdgcn_global_load_lds((const unsigned*)((const char*)(gbase) + voffB[_i]), (LAS unsigned*)(lds + (bufoff) + ldsw + _i * 8192), 16, 0, 0); } while (0)
; #define PG8_STAGE_A(bufoff, gbase, VO, h) do { _Pragma("unroll") for (int _i = 0; _i < 2; ++_i) \
;         __builtin_amdgcn_global_load_lds((const unsigned*)((const char*)(gbase) + (VO)[h][_i]), (LAS unsigned*)(lds + (bufoff) + ldsw + _i * 8192), 16, 0, 0); } while (0)
; #define PG8_WAIT_L(n) asm volatile("s_waitcnt lgkmcnt(" #n ")" ::: "memory")
; #define PG8_WAIT_VX(rx) do { if (rx) asm volatile("s_waitcnt vmcnt(%0)" :: "n"(8 + Epi::NVM) : "memory"); else asm volatile("s_waitcnt vmcnt(8)" ::: "memory"); } while (0)
; #define PG8_BAR __builtin_amdgcn_s_barrier()
; #define PG8_SCHED __builtin_amdgcn_sched_barrier(0)
;     ...
;             PG8_LDB(B0, 0, 0); PG8_LDB(B1, 0, 1); PG8_SCHED; PG8_LDA(At, 0, 0); if (!rx) PG8_STAGE_A(PG8_SA(1, 1), a1, voffA, 1);
;             PG8_WAIT_VX(rx); PG8_WAIT_L(0); PG8_BAR; PG8_MMA(0, 0, At, B0); PG8_MMA(0, 1, At, B1); PG8_BAR; PG8_SCHED;
;             PG8_LDA(At, 0, 1); PG8_STAGE_B(PG8_SB(0, 0), b2); PG8_STAGE_B(PG8_SB(0, 1), b2 + hstepB); PG8_STAGE_A(PG8_SA(0, 0), a2, vo2, 0);
;             PG8_WAIT_VX(rx); PG8_WAIT_L(0); PG8_BAR; PG8_MMA(1, 0, At, B0); PG8_MMA(1, 1, At, B1); PG8_BAR; PG8_SCHED;
.LBB0_1415:
	s_add_u32 s7, s24, 0x100
	s_addc_u32 s26, s25, 0
	s_and_b64 s[24:25], s[2:3], exec
	s_cselect_b32 s27, s11, s26
	s_cselect_b32 s26, s10, s7
	s_lshl_b32 s5, s5, 18
	s_add_u32 s5, s14, s5
	s_addc_u32 s7, s15, 0
	s_add_u32 s5, s5, 0x80000
	s_addc_u32 s7, s7, 0
	s_waitcnt lgkmcnt(0)
	s_and_b64 s[2:3], s[2:3], exec
	s_cselect_b32 s25, s9, s7
	s_cselect_b32 s24, s8, s5
	s_barrier
	s_setprio 1
	s_waitcnt lgkmcnt(0)
	v_mfma_scale_f32_16x16x128_f8f6f4 v[190:193], v[24:31], v[56:63], v[190:193], v226, v228 op_sel_hi:[0,0,0]
	v_mfma_scale_f32_16x16x128_f8f6f4 v[186:189], v[16:23], v[56:63], v[186:189], v226, v228 op_sel_hi:[0,0,0]
	v_mfma_scale_f32_16x16x128_f8f6f4 v[178:181], v[24:31], v[48:55], v[178:181], v226, v228 op_sel_hi:[0,0,0]
	v_mfma_scale_f32_16x16x128_f8f6f4 v[170:173], v[16:23], v[48:55], v[170:173], v226, v228 op_sel_hi:[0,0,0]
	v_mfma_scale_f32_16x16x128_f8f6f4 v[162:165], v[24:31], v[40:47], v[162:165], v226, v228 op_sel_hi:[0,0,0]
	v_mfma_scale_f32_16x16x128_f8f6f4 v[154:157], v[16:23], v[40:47], v[154:157], v226, v228 op_sel_hi:[0,0,0]
	v_mfma_scale_f32_16x16x128_f8f6f4 v[146:149], v[24:31], v[32:39], v[146:149], v226, v228 op_sel_hi:[0,0,0]
	v_mfma_scale_f32_16x16x128_f8f6f4 v[138:141], v[16:23], v[32:39], v[138:141], v226, v228 op_sel_hi:[0,0,0]
	s_setprio 0
	s_setprio 1
	v_mfma_scale_f32_16x16x128_f8f6f4 v[182:185], v[8:15], v[56:63], v[182:185], v226, v228 op_sel_hi:[0,0,0]
	v_mfma_scale_f32_16x16x128_f8f6f4 v[174:177], v[0:7], v[56:63], v[174:177], v226, v228 op_sel_hi:[0,0,0]
	v_mfma_scale_f32_16x16x128_f8f6f4 v[166:169], v[8:15], v[48:55], v[166:169], v226, v228 op_sel_hi:[0,0,0]
	v_mfma_scale_f32_16x16x128_f8f6f4 v[158:161], v[0:7], v[48:55], v[158:161], v226, v228 op_sel_hi:[0,0,0]
	v_mfma_scale_f32_16x16x128_f8f6f4 v[150:153], v[8:15], v[40:47], v[150:153], v226, v228 op_sel_hi:[0,0,0]
	v_mfma_scale_f32_16x16x128_f8f6f4 v[142:145], v[0:7], v[40:47], v[142:145], v226, v228 op_sel_hi:[0,0,0]
	v_mfma_scale_f32_16x16x128_f8f6f4 v[134:137], v[8:15], v[32:39], v[134:137], v226, v228 op_sel_hi:[0,0,0]
	v_mfma_scale_f32_16x16x128_f8f6f4 v[130:133], v[0:7], v[32:39], v[130:133], v226, v228 op_sel_hi:[0,0,0]
	s_setprio 0
	s_barrier
	s_mov_b32 m0, s35
	v_lshl_add_u64 v[206:207], s[24:25], 0, v[64:65]
	ds_read_b128 v[56:59], v212 offset:16384
	ds_read_b128 v[60:63], v212 offset:17408
	ds_read_b128 v[48:51], v212 offset:18432
	ds_read_b128 v[52:55], v212 offset:19456
	ds_read_b128 v[40:43], v212 offset:20480
	ds_read_b128 v[44:47], v212 offset:21504
	ds_read_b128 v[32:35], v212 offset:22528
	ds_read_b128 v[36:39], v212 offset:23552
	s_and_b64 vcc, exec, s[28:29]
	s_cbranch_vccz .Lmy_p7_s0_w
	s_waitcnt vmcnt(12)
	s_branch .Lmy_p7_s0_go
.Lmy_p7_s0_w:
	s_waitcnt vmcnt(4)
.Lmy_p7_s0_go:
	s_add_u32 s2, s24, 0x200
	ds_write_b128 v248, v[232:235] offset:32768
	ds_write_b128 v248, v[236:239] offset:40960
	ds_write_b128 v248, v[240:243] offset:49152
	ds_write_b128 v248, v[244:247] offset:57344
	global_load_dwordx4 v[232:235], v[206:207], off
	v_lshl_add_u64 v[206:207], s[24:25], 0, v[198:199]
	s_mov_b32 m0, s36
	s_addc_u32 s3, s25, 0
	global_load_dwordx4 v[236:239], v[206:207], off
	v_lshl_add_u64 v[206:207], s[2:3], 0, v[64:65]
	s_mov_b32 m0, s37
	v_lshl_add_u64 v[208:209], s[26:27], 0, v[196:197]
	global_load_dwordx4 v[240:243], v[206:207], off
	v_lshl_add_u64 v[206:207], s[2:3], 0, v[198:199]
	s_mov_b32 m0, s38
	v_cndmask_b32_e64 v213, 0, 1, s[28:29]
	global_load_dwordx4 v[244:247], v[206:207], off
	v_lshl_add_u64 v[206:207], s[26:27], 0, v[202:203]
	s_mov_b32 m0, s13
	v_cmp_ne_u32_e64 s[2:3], 1, v213
	global_load_lds_dwordx4 v[206:207], off
	s_mov_b32 m0, s39
	s_andn2_b64 vcc, exec, s[28:29]
	global_load_lds_dwordx4 v[208:209], off
	s_cbranch_vccnz .LBB0_1420
	s_waitcnt vmcnt(16)
	s_cbranch_execnz .LBB0_1418
